# neighbourhood attention: the 16 exec-masked bias lookups per half tile (ds_read + wait each) replaced by 16 unconditional ds_reads, one wait and v_cndmask
# speedup vs baseline: 1.0110x; 1.0025x over previous
.LBB0_759:
	s_andn2_b64 vcc, exec, s[16:17]
	s_cbranch_vccnz .LBB0_793
	v_mov_b32_e32 v241, v190
	v_mov_b32_e32 v67, 0xff800000
	v_add_u32_e32 v242, 16, v241
	v_mov_b32_e32 v222, 0xff800000
	ds_read_b32 v66, v237
	ds_read_b32 v67, v237 offset:4
	ds_read_b32 v68, v237 offset:8
	ds_read_b32 v69, v237 offset:12
	ds_read_b32 v70, v237 offset:32
	ds_read_b32 v71, v237 offset:36
	ds_read_b32 v72, v237 offset:40
	ds_read_b32 v73, v237 offset:44
	ds_read_b32 v74, v237 offset:64
	ds_read_b32 v75, v237 offset:68
	ds_read_b32 v76, v237 offset:72
	ds_read_b32 v77, v237 offset:76
	ds_read_b32 v78, v237 offset:96
	ds_read_b32 v79, v237 offset:100
	ds_read_b32 v80, v237 offset:104
	ds_read_b32 v81, v237 offset:108
	s_waitcnt lgkmcnt(0)
	v_cmp_ge_i32_e32 vcc, v181, v241
	v_cmp_lt_i32_e64 s[16:17], v181, v242
	s_and_b64 vcc, vcc, s[16:17]
	v_fmac_f32_e32 v66, 0x3e0293ee, v82
	v_cndmask_b32_e32 v66, v222, v66, vcc
	v_cmp_ge_i32_e32 vcc, v203, v241
	v_cmp_lt_i32_e64 s[16:17], v203, v242
	s_and_b64 vcc, vcc, s[16:17]
	v_fmac_f32_e32 v67, 0x3e0293ee, v83
	v_cndmask_b32_e32 v67, v222, v67, vcc
	v_cmp_ge_i32_e32 vcc, v204, v241
	v_cmp_lt_i32_e64 s[16:17], v204, v242
	s_and_b64 vcc, vcc, s[16:17]
	v_fmac_f32_e32 v68, 0x3e0293ee, v84
	v_cndmask_b32_e32 v68, v222, v68, vcc
	v_cmp_ge_i32_e32 vcc, v205, v241
	v_cmp_lt_i32_e64 s[16:17], v205, v242
	s_and_b64 vcc, vcc, s[16:17]
	v_fmac_f32_e32 v69, 0x3e0293ee, v85
	v_cndmask_b32_e32 v69, v222, v69, vcc
	v_cmp_ge_i32_e32 vcc, v206, v241
	v_cmp_lt_i32_e64 s[16:17], v206, v242
	s_and_b64 vcc, vcc, s[16:17]
	v_fmac_f32_e32 v70, 0x3e0293ee, v86
	v_cndmask_b32_e32 v70, v222, v70, vcc
	v_cmp_ge_i32_e32 vcc, v207, v241
	v_cmp_lt_i32_e64 s[16:17], v207, v242
	s_and_b64 vcc, vcc, s[16:17]
	v_fmac_f32_e32 v71, 0x3e0293ee, v87
	v_cndmask_b32_e32 v71, v222, v71, vcc
	v_cmp_ge_i32_e32 vcc, v208, v241
	v_cmp_lt_i32_e64 s[16:17], v208, v242
	s_and_b64 vcc, vcc, s[16:17]
	v_fmac_f32_e32 v72, 0x3e0293ee, v88
	v_cndmask_b32_e32 v72, v222, v72, vcc
	v_cmp_ge_i32_e32 vcc, v209, v241
	v_cmp_lt_i32_e64 s[16:17], v209, v242
	s_and_b64 vcc, vcc, s[16:17]
	v_fmac_f32_e32 v73, 0x3e0293ee, v89
	v_cndmask_b32_e32 v73, v222, v73, vcc
	v_cmp_ge_i32_e32 vcc, v210, v241
	v_cmp_lt_i32_e64 s[16:17], v181, v241
	s_and_b64 vcc, vcc, s[16:17]
	v_fmac_f32_e32 v74, 0x3e0293ee, v90
	v_cndmask_b32_e32 v74, v222, v74, vcc
	v_cmp_ge_i32_e32 vcc, v211, v241
	v_cmp_lt_i32_e64 s[16:17], v211, v242
	s_and_b64 vcc, vcc, s[16:17]
	v_fmac_f32_e32 v75, 0x3e0293ee, v91
	v_cndmask_b32_e32 v75, v222, v75, vcc
	v_cmp_ge_i32_e32 vcc, v212, v241
	v_cmp_lt_i32_e64 s[16:17], v212, v242
	s_and_b64 vcc, vcc, s[16:17]
	v_fmac_f32_e32 v76, 0x3e0293ee, v92
	v_cndmask_b32_e32 v76, v222, v76, vcc
	v_cmp_ge_i32_e32 vcc, v213, v241
	v_cmp_lt_i32_e64 s[16:17], v213, v242
	s_and_b64 vcc, vcc, s[16:17]
	v_fmac_f32_e32 v77, 0x3e0293ee, v93
	v_cndmask_b32_e32 v77, v222, v77, vcc
	v_cmp_ge_i32_e32 vcc, v214, v241
	v_cmp_lt_i32_e64 s[16:17], v214, v242
	s_and_b64 vcc, vcc, s[16:17]
	v_fmac_f32_e32 v78, 0x3e0293ee, v94
	v_cndmask_b32_e32 v78, v222, v78, vcc
	v_cmp_ge_i32_e32 vcc, v215, v241
	v_cmp_lt_i32_e64 s[16:17], v215, v242
	s_and_b64 vcc, vcc, s[16:17]
	v_fmac_f32_e32 v79, 0x3e0293ee, v95
	v_cndmask_b32_e32 v79, v222, v79, vcc
	v_cmp_ge_i32_e32 vcc, v216, v241
	v_cmp_lt_i32_e64 s[16:17], v216, v242
	s_and_b64 vcc, vcc, s[16:17]
	v_fmac_f32_e32 v80, 0x3e0293ee, v96
	v_cndmask_b32_e32 v80, v222, v80, vcc
	v_cmp_ge_i32_e32 vcc, v217, v241
	v_cmp_lt_i32_e64 s[16:17], v217, v242
	s_and_b64 vcc, vcc, s[16:17]
	v_fmac_f32_e32 v81, 0x3e0293ee, v97
	v_cndmask_b32_e32 v81, v222, v81, vcc

.LBB0_799:
	s_andn2_b64 vcc, exec, s[16:17]
	s_cbranch_vccnz .LBB0_833
	v_mov_b32_e32 v245, v190
	v_mov_b32_e32 v67, 0xff800000
	v_add_u32_e32 v246, 16, v245
	v_mov_b32_e32 v222, 0xff800000
	ds_read_b32 v66, v237 offset:128
	ds_read_b32 v67, v237 offset:132
	ds_read_b32 v68, v237 offset:136
	ds_read_b32 v69, v237 offset:140
	ds_read_b32 v70, v237 offset:160
	ds_read_b32 v71, v237 offset:164
	ds_read_b32 v72, v237 offset:168
	ds_read_b32 v73, v237 offset:172
	ds_read_b32 v74, v237 offset:192
	ds_read_b32 v75, v237 offset:196
	ds_read_b32 v76, v237 offset:200
	ds_read_b32 v77, v237 offset:204
	ds_read_b32 v78, v237 offset:224
	ds_read_b32 v79, v237 offset:228
	ds_read_b32 v80, v237 offset:232
	ds_read_b32 v81, v237 offset:236
	s_waitcnt lgkmcnt(0)
	v_cmp_ge_i32_e32 vcc, v219, v245
	v_cmp_lt_i32_e64 s[12:13], v219, v246
	s_and_b64 vcc, vcc, s[12:13]
	v_fmac_f32_e32 v66, 0x3e0293ee, v82
	v_cndmask_b32_e32 v66, v222, v66, vcc
	v_cmp_ge_i32_e32 vcc, v220, v245
	v_cmp_lt_i32_e64 s[12:13], v220, v246
	s_and_b64 vcc, vcc, s[12:13]
	v_fmac_f32_e32 v67, 0x3e0293ee, v83
	v_cndmask_b32_e32 v67, v222, v67, vcc
	v_cmp_ge_i32_e32 vcc, v221, v245
	v_cmp_lt_i32_e64 s[12:13], v221, v246
	s_and_b64 vcc, vcc, s[12:13]
	v_fmac_f32_e32 v68, 0x3e0293ee, v84
	v_cndmask_b32_e32 v68, v222, v68, vcc
	v_cmp_ge_i32_e32 vcc, v223, v245
	v_cmp_lt_i32_e64 s[12:13], v223, v246
	s_and_b64 vcc, vcc, s[12:13]
	v_fmac_f32_e32 v69, 0x3e0293ee, v85
	v_cndmask_b32_e32 v69, v222, v69, vcc
	v_cmp_ge_i32_e32 vcc, v224, v245
	v_cmp_lt_i32_e64 s[12:13], v224, v246
	s_and_b64 vcc, vcc, s[12:13]
	v_fmac_f32_e32 v70, 0x3e0293ee, v86
	v_cndmask_b32_e32 v70, v222, v70, vcc
	v_cmp_ge_i32_e32 vcc, v225, v245
	v_cmp_lt_i32_e64 s[12:13], v225, v246
	s_and_b64 vcc, vcc, s[12:13]
	v_fmac_f32_e32 v71, 0x3e0293ee, v87
	v_cndmask_b32_e32 v71, v222, v71, vcc
	v_cmp_ge_i32_e32 vcc, v226, v245
	v_cmp_lt_i32_e64 s[12:13], v226, v246
	s_and_b64 vcc, vcc, s[12:13]
	v_fmac_f32_e32 v72, 0x3e0293ee, v88
	v_cndmask_b32_e32 v72, v222, v72, vcc
	v_cmp_ge_i32_e32 vcc, v227, v245
	v_cmp_lt_i32_e64 s[12:13], v227, v246
	s_and_b64 vcc, vcc, s[12:13]
	v_fmac_f32_e32 v73, 0x3e0293ee, v89
	v_cndmask_b32_e32 v73, v222, v73, vcc
	v_cmp_ge_i32_e32 vcc, v228, v245
	v_cmp_lt_i32_e64 s[12:13], v228, v246
	s_and_b64 vcc, vcc, s[12:13]
	v_fmac_f32_e32 v74, 0x3e0293ee, v90
	v_cndmask_b32_e32 v74, v222, v74, vcc
	v_cmp_ge_i32_e32 vcc, v229, v245
	v_cmp_lt_i32_e64 s[12:13], v229, v246
	s_and_b64 vcc, vcc, s[12:13]
	v_fmac_f32_e32 v75, 0x3e0293ee, v91
	v_cndmask_b32_e32 v75, v222, v75, vcc
	v_cmp_ge_i32_e32 vcc, v230, v245
	v_cmp_lt_i32_e64 s[12:13], v230, v246
	s_and_b64 vcc, vcc, s[12:13]
	v_fmac_f32_e32 v76, 0x3e0293ee, v92
	v_cndmask_b32_e32 v76, v222, v76, vcc
	v_cmp_ge_i32_e32 vcc, v231, v245
	v_cmp_lt_i32_e64 s[12:13], v231, v246
	s_and_b64 vcc, vcc, s[12:13]
	v_fmac_f32_e32 v77, 0x3e0293ee, v93
	v_cndmask_b32_e32 v77, v222, v77, vcc
	v_cmp_ge_i32_e32 vcc, v232, v245
	v_cmp_lt_i32_e64 s[12:13], v232, v246
	s_and_b64 vcc, vcc, s[12:13]
	v_fmac_f32_e32 v78, 0x3e0293ee, v94
	v_cndmask_b32_e32 v78, v222, v78, vcc
	v_cmp_ge_i32_e32 vcc, v233, v245
	v_cmp_lt_i32_e64 s[12:13], v233, v246
	s_and_b64 vcc, vcc, s[12:13]
	v_fmac_f32_e32 v79, 0x3e0293ee, v95
	v_cndmask_b32_e32 v79, v222, v79, vcc
	v_cmp_ge_i32_e32 vcc, v234, v245
	v_cmp_lt_i32_e64 s[12:13], v234, v246
	s_and_b64 vcc, vcc, s[12:13]
	v_fmac_f32_e32 v80, 0x3e0293ee, v96
	v_cndmask_b32_e32 v80, v222, v80, vcc
	v_cmp_ge_i32_e32 vcc, v235, v245
	v_cmp_lt_i32_e64 s[12:13], v235, v246
	s_and_b64 vcc, vcc, s[12:13]
	v_fmac_f32_e32 v81, 0x3e0293ee, v97
	v_cndmask_b32_e32 v81, v222, v81, vcc

.LBB0_2043:
	s_andn2_b64 vcc, exec, s[16:17]
	s_cbranch_vccnz .LBB0_2077
	v_mov_b32_e32 v14, v192
	v_mov_b32_e32 v83, 0xff800000
	v_add_u32_e32 v15, 16, v14
	v_mov_b32_e32 v222, 0xff800000
	ds_read_b32 v82, v240
	ds_read_b32 v83, v240 offset:4
	ds_read_b32 v84, v240 offset:8
	ds_read_b32 v85, v240 offset:12
	ds_read_b32 v86, v240 offset:32
	ds_read_b32 v87, v240 offset:36
	ds_read_b32 v88, v240 offset:40
	ds_read_b32 v89, v240 offset:44
	ds_read_b32 v90, v240 offset:64
	ds_read_b32 v91, v240 offset:68
	ds_read_b32 v92, v240 offset:72
	ds_read_b32 v93, v240 offset:76
	ds_read_b32 v94, v240 offset:96
	ds_read_b32 v95, v240 offset:100
	ds_read_b32 v96, v240 offset:104
	ds_read_b32 v97, v240 offset:108
	s_waitcnt lgkmcnt(0)
	v_cmp_ge_i32_e32 vcc, v194, v14
	v_cmp_lt_i32_e64 s[16:17], v194, v15
	s_and_b64 vcc, vcc, s[16:17]
	v_fmac_f32_e32 v82, 0x3e0293ee, v98
	v_cndmask_b32_e32 v82, v222, v82, vcc
	v_cmp_ge_i32_e32 vcc, v206, v14
	v_cmp_lt_i32_e64 s[16:17], v206, v15
	s_and_b64 vcc, vcc, s[16:17]
	v_fmac_f32_e32 v83, 0x3e0293ee, v99
	v_cndmask_b32_e32 v83, v222, v83, vcc
	v_cmp_ge_i32_e32 vcc, v207, v14
	v_cmp_lt_i32_e64 s[16:17], v207, v15
	s_and_b64 vcc, vcc, s[16:17]
	v_fmac_f32_e32 v84, 0x3e0293ee, v100
	v_cndmask_b32_e32 v84, v222, v84, vcc
	v_cmp_ge_i32_e32 vcc, v208, v14
	v_cmp_lt_i32_e64 s[16:17], v208, v15
	s_and_b64 vcc, vcc, s[16:17]
	v_fmac_f32_e32 v85, 0x3e0293ee, v101
	v_cndmask_b32_e32 v85, v222, v85, vcc
	v_cmp_ge_i32_e32 vcc, v209, v14
	v_cmp_lt_i32_e64 s[16:17], v209, v15
	s_and_b64 vcc, vcc, s[16:17]
	v_fmac_f32_e32 v86, 0x3e0293ee, v102
	v_cndmask_b32_e32 v86, v222, v86, vcc
	v_cmp_ge_i32_e32 vcc, v210, v14
	v_cmp_lt_i32_e64 s[16:17], v210, v15
	s_and_b64 vcc, vcc, s[16:17]
	v_fmac_f32_e32 v87, 0x3e0293ee, v103
	v_cndmask_b32_e32 v87, v222, v87, vcc
	v_cmp_ge_i32_e32 vcc, v211, v14
	v_cmp_lt_i32_e64 s[16:17], v211, v15
	s_and_b64 vcc, vcc, s[16:17]
	v_fmac_f32_e32 v88, 0x3e0293ee, v104
	v_cndmask_b32_e32 v88, v222, v88, vcc
	v_cmp_ge_i32_e32 vcc, v212, v14
	v_cmp_lt_i32_e64 s[16:17], v212, v15
	s_and_b64 vcc, vcc, s[16:17]
	v_fmac_f32_e32 v89, 0x3e0293ee, v105
	v_cndmask_b32_e32 v89, v222, v89, vcc
	v_cmp_ge_i32_e32 vcc, v213, v14
	v_cmp_lt_i32_e64 s[16:17], v194, v14
	s_and_b64 vcc, vcc, s[16:17]
	v_fmac_f32_e32 v90, 0x3e0293ee, v106
	v_cndmask_b32_e32 v90, v222, v90, vcc
	v_cmp_ge_i32_e32 vcc, v214, v14
	v_cmp_lt_i32_e64 s[16:17], v214, v15
	s_and_b64 vcc, vcc, s[16:17]
	v_fmac_f32_e32 v91, 0x3e0293ee, v107
	v_cndmask_b32_e32 v91, v222, v91, vcc
	v_cmp_ge_i32_e32 vcc, v215, v14
	v_cmp_lt_i32_e64 s[16:17], v215, v15
	s_and_b64 vcc, vcc, s[16:17]
	v_fmac_f32_e32 v92, 0x3e0293ee, v108
	v_cndmask_b32_e32 v92, v222, v92, vcc
	v_cmp_ge_i32_e32 vcc, v216, v14
	v_cmp_lt_i32_e64 s[16:17], v216, v15
	s_and_b64 vcc, vcc, s[16:17]
	v_fmac_f32_e32 v93, 0x3e0293ee, v109
	v_cndmask_b32_e32 v93, v222, v93, vcc
	v_cmp_ge_i32_e32 vcc, v217, v14
	v_cmp_lt_i32_e64 s[16:17], v217, v15
	s_and_b64 vcc, vcc, s[16:17]
	v_fmac_f32_e32 v94, 0x3e0293ee, v110
	v_cndmask_b32_e32 v94, v222, v94, vcc
	v_cmp_ge_i32_e32 vcc, v218, v14
	v_cmp_lt_i32_e64 s[16:17], v218, v15
	s_and_b64 vcc, vcc, s[16:17]
	v_fmac_f32_e32 v95, 0x3e0293ee, v111
	v_cndmask_b32_e32 v95, v222, v95, vcc
	v_cmp_ge_i32_e32 vcc, v219, v14
	v_cmp_lt_i32_e64 s[16:17], v219, v15
	s_and_b64 vcc, vcc, s[16:17]
	v_fmac_f32_e32 v96, 0x3e0293ee, v112
	v_cndmask_b32_e32 v96, v222, v96, vcc
	v_cmp_ge_i32_e32 vcc, v220, v14
	v_cmp_lt_i32_e64 s[16:17], v220, v15
	s_and_b64 vcc, vcc, s[16:17]
	v_fmac_f32_e32 v97, 0x3e0293ee, v113
	v_cndmask_b32_e32 v97, v222, v97, vcc

.LBB0_2083:
	s_andn2_b64 vcc, exec, s[16:17]
	s_cbranch_vccnz .LBB0_2117
	v_mov_b32_e32 v245, v192
	v_mov_b32_e32 v83, 0xff800000
	v_add_u32_e32 v246, 16, v245
	v_mov_b32_e32 v222, 0xff800000
	ds_read_b32 v82, v240 offset:128
	ds_read_b32 v83, v240 offset:132
	ds_read_b32 v84, v240 offset:136
	ds_read_b32 v85, v240 offset:140
	ds_read_b32 v86, v240 offset:160
	ds_read_b32 v87, v240 offset:164
	ds_read_b32 v88, v240 offset:168
	ds_read_b32 v89, v240 offset:172
	ds_read_b32 v90, v240 offset:192
	ds_read_b32 v91, v240 offset:196
	ds_read_b32 v92, v240 offset:200
	ds_read_b32 v93, v240 offset:204
	ds_read_b32 v94, v240 offset:224
	ds_read_b32 v95, v240 offset:228
	ds_read_b32 v96, v240 offset:232
	ds_read_b32 v97, v240 offset:236
	s_waitcnt lgkmcnt(0)
	v_cmp_ge_i32_e32 vcc, v223, v245
	v_cmp_lt_i32_e64 s[12:13], v223, v246
	s_and_b64 vcc, vcc, s[12:13]
	v_fmac_f32_e32 v82, 0x3e0293ee, v98
	v_cndmask_b32_e32 v82, v222, v82, vcc
	v_cmp_ge_i32_e32 vcc, v224, v245
	v_cmp_lt_i32_e64 s[12:13], v224, v246
	s_and_b64 vcc, vcc, s[12:13]
	v_fmac_f32_e32 v83, 0x3e0293ee, v99
	v_cndmask_b32_e32 v83, v222, v83, vcc
	v_cmp_ge_i32_e32 vcc, v225, v245
	v_cmp_lt_i32_e64 s[12:13], v225, v246
	s_and_b64 vcc, vcc, s[12:13]
	v_fmac_f32_e32 v84, 0x3e0293ee, v100
	v_cndmask_b32_e32 v84, v222, v84, vcc
	v_cmp_ge_i32_e32 vcc, v226, v245
	v_cmp_lt_i32_e64 s[12:13], v226, v246
	s_and_b64 vcc, vcc, s[12:13]
	v_fmac_f32_e32 v85, 0x3e0293ee, v101
	v_cndmask_b32_e32 v85, v222, v85, vcc
	v_cmp_ge_i32_e32 vcc, v227, v245
	v_cmp_lt_i32_e64 s[12:13], v227, v246
	s_and_b64 vcc, vcc, s[12:13]
	v_fmac_f32_e32 v86, 0x3e0293ee, v102
	v_cndmask_b32_e32 v86, v222, v86, vcc
	v_cmp_ge_i32_e32 vcc, v228, v245
	v_cmp_lt_i32_e64 s[12:13], v228, v246
	s_and_b64 vcc, vcc, s[12:13]
	v_fmac_f32_e32 v87, 0x3e0293ee, v103
	v_cndmask_b32_e32 v87, v222, v87, vcc
	v_cmp_ge_i32_e32 vcc, v229, v245
	v_cmp_lt_i32_e64 s[12:13], v229, v246
	s_and_b64 vcc, vcc, s[12:13]
	v_fmac_f32_e32 v88, 0x3e0293ee, v104
	v_cndmask_b32_e32 v88, v222, v88, vcc
	v_cmp_ge_i32_e32 vcc, v230, v245
	v_cmp_lt_i32_e64 s[12:13], v230, v246
	s_and_b64 vcc, vcc, s[12:13]
	v_fmac_f32_e32 v89, 0x3e0293ee, v105
	v_cndmask_b32_e32 v89, v222, v89, vcc
	v_cmp_ge_i32_e32 vcc, v231, v245
	v_cmp_lt_i32_e64 s[12:13], v231, v246
	s_and_b64 vcc, vcc, s[12:13]
	v_fmac_f32_e32 v90, 0x3e0293ee, v106
	v_cndmask_b32_e32 v90, v222, v90, vcc
	v_cmp_ge_i32_e32 vcc, v232, v245
	v_cmp_lt_i32_e64 s[12:13], v232, v246
	s_and_b64 vcc, vcc, s[12:13]
	v_fmac_f32_e32 v91, 0x3e0293ee, v107
	v_cndmask_b32_e32 v91, v222, v91, vcc
	v_cmp_ge_i32_e32 vcc, v233, v245
	v_cmp_lt_i32_e64 s[12:13], v233, v246
	s_and_b64 vcc, vcc, s[12:13]
	v_fmac_f32_e32 v92, 0x3e0293ee, v108
	v_cndmask_b32_e32 v92, v222, v92, vcc
	v_cmp_ge_i32_e32 vcc, v234, v245
	v_cmp_lt_i32_e64 s[12:13], v234, v246
	s_and_b64 vcc, vcc, s[12:13]
	v_fmac_f32_e32 v93, 0x3e0293ee, v109
	v_cndmask_b32_e32 v93, v222, v93, vcc
	v_cmp_ge_i32_e32 vcc, v235, v245
	v_cmp_lt_i32_e64 s[12:13], v235, v246
	s_and_b64 vcc, vcc, s[12:13]
	v_fmac_f32_e32 v94, 0x3e0293ee, v110
	v_cndmask_b32_e32 v94, v222, v94, vcc
	v_cmp_ge_i32_e32 vcc, v236, v245
	v_cmp_lt_i32_e64 s[12:13], v236, v246
	s_and_b64 vcc, vcc, s[12:13]
	v_fmac_f32_e32 v95, 0x3e0293ee, v111
	v_cndmask_b32_e32 v95, v222, v95, vcc
	v_cmp_ge_i32_e32 vcc, v237, v245
	v_cmp_lt_i32_e64 s[12:13], v237, v246
	s_and_b64 vcc, vcc, s[12:13]
	v_fmac_f32_e32 v96, 0x3e0293ee, v112
	v_cndmask_b32_e32 v96, v222, v96, vcc
	v_cmp_ge_i32_e32 vcc, v238, v245
	v_cmp_lt_i32_e64 s[12:13], v238, v246
	s_and_b64 vcc, vcc, s[12:13]
	v_fmac_f32_e32 v97, 0x3e0293ee, v113
	v_cndmask_b32_e32 v97, v222, v97, vcc
